# ROUTE: the vmcnt(0) that guarded only the non-uniform-modulation parameter loads moved into that branch, so the per-chunk e4m3 stores no longer drain before the next chunk (on top of v34)
# baseline (speedup 1.0000x reference)
.LBB0_1628:
	s_add_i32 s54, s26, s51
	v_cndmask_b32_e64 v50, 0, 1, s[36:37]
	s_cmp_lt_i32 s54, s23
	v_cmp_ne_u32_e64 s[10:11], 1, v50
	s_cbranch_scc0 .LBB0_1655
	s_waitcnt vmcnt(15)
	v_lshlrev_b32_e32 v132, 16, v82
	v_and_b32_e32 v133, 0xffff0000, v82
	s_waitcnt vmcnt(14)
	v_lshlrev_b32_e32 v128, 16, v84
	v_and_b32_e32 v129, 0xffff0000, v84
	s_add_i32 s44, s52, s51
	v_lshlrev_b32_e32 v134, 16, v83
	v_and_b32_e32 v135, 0xffff0000, v83
	v_pk_mul_f32 v[50:51], v[132:133], v[132:133]
	v_lshlrev_b32_e32 v126, 16, v85
	v_and_b32_e32 v127, 0xffff0000, v85
	v_pk_mul_f32 v[130:131], v[128:129], v[128:129]
	s_waitcnt vmcnt(13)
	v_lshlrev_b32_e32 v124, 16, v86
	v_and_b32_e32 v125, 0xffff0000, v86
	v_pk_mul_f32 v[52:53], v[134:135], v[134:135]
	v_pk_mul_f32 v[136:137], v[126:127], v[126:127]
	v_lshlrev_b32_e32 v122, 16, v87
	v_and_b32_e32 v123, 0xffff0000, v87
	v_pk_mul_f32 v[138:139], v[124:125], v[124:125]
	v_add_f32_e32 v130, v130, v131
	v_add_f32_e32 v50, v50, v51
	s_ashr_i32 s45, s44, 31
	v_pk_mul_f32 v[164:165], v[122:123], v[122:123]
	v_add_f32_e32 v130, v130, v136
	v_add_f32_e32 v50, v50, v52
	v_add_f32_e32 v51, v138, v139
	s_lshr_b32 s40, s45, 20
	s_waitcnt vmcnt(12)
	v_lshlrev_b32_e32 v120, 16, v88
	v_and_b32_e32 v121, 0xffff0000, v88
	v_add_f32_e32 v130, v137, v130
	v_add_f32_e32 v50, v53, v50
	v_add_f32_e32 v51, v51, v164
	s_add_i32 s40, s44, s40
	v_lshlrev_b32_e32 v118, 16, v89
	v_and_b32_e32 v119, 0xffff0000, v89
	v_pk_mul_f32 v[166:167], v[120:121], v[120:121]
	v_add_f32_e32 v50, v50, v130
	v_add_f32_e32 v51, v165, v51
	s_ashr_i32 s40, s40, 12
	v_pk_mul_f32 v[168:169], v[118:119], v[118:119]
	v_add_f32_e32 v50, v50, v51
	v_add_f32_e32 v51, v166, v167
	s_cmp_lt_i32 s44, 0x8000
	v_add_f32_e32 v51, v51, v168
	s_cselect_b32 s40, s40, 8
	v_add_f32_e32 v51, v169, v51
	s_ashr_i32 s41, s40, 31
	v_add_f32_e32 v50, v50, v51
	s_add_u32 s40, s49, s40
	s_addc_u32 s41, s48, s41
	v_add_f32_dpp v50, v50, v50 row_ror:1 row_mask:0xf bank_mask:0xf bound_ctrl:1
	s_mulk_i32 s41, 0x6000
	s_mul_hi_u32 s42, s40, 0x6000
	v_add_f32_dpp v50, v50, v50 row_ror:2 row_mask:0xf bank_mask:0xf bound_ctrl:1
	s_add_i32 s42, s42, s41
	s_mulk_i32 s40, 0x6000
	v_add_f32_dpp v50, v50, v50 row_ror:4 row_mask:0xf bank_mask:0xf bound_ctrl:1
	s_add_u32 s43, s30, s40
	s_addc_u32 s55, s31, s42
	v_add_f32_dpp v50, v50, v50 row_ror:8 row_mask:0xf bank_mask:0xf bound_ctrl:1
	v_mov_b32_e32 v51, v50
	s_nop 1
	v_permlane16_swap_b32_e32 v50, v51
	s_add_u32 s40, s43, 0x103000
	v_add_f32_e32 v130, v50, v51
	s_addc_u32 s41, s55, 0
	v_mov_b32_e32 v131, v130
	s_add_u32 s42, s43, 0x104000
	s_nop 0
	v_permlane32_swap_b32_e32 v130, v131
	s_addc_u32 s43, s55, 0
	s_and_b64 vcc, exec, s[10:11]
	v_mov_b64_e32 v[138:139], v[66:67]
	v_mov_b64_e32 v[136:137], v[68:69]
	v_mov_b32_e32 v50, v34
	v_mov_b32_e32 v51, v35
	v_mov_b32_e32 v52, v36
	v_mov_b32_e32 v53, v37
	s_cbranch_vccnz .LBB0_1631
	v_lshlrev_b32_e32 v50, 4, v54
	global_load_dwordx4 v[136:139], v50, s[42:43]
	global_load_dwordx4 v[164:167], v[64:65], off
	s_nop 0
	global_load_dwordx4 v[50:53], v50, s[40:41]
	s_waitcnt vmcnt(2)
	v_pk_add_f32 v[136:137], v[136:137], 1.0 op_sel_hi:[1,0]
	v_pk_add_f32 v[168:169], v[138:139], 1.0 op_sel_hi:[1,0]
	s_waitcnt vmcnt(1)
	v_pk_mul_f32 v[138:139], v[164:165], v[136:137]
	v_pk_mul_f32 v[136:137], v[166:167], v[168:169]
	s_waitcnt vmcnt(0)
.LBB0_1631:
	v_add_f32_e32 v130, v130, v131
	v_fmamk_f32 v130, v130, 0x3a800000, v237
	s_mov_b32 s55, 0x800000
	v_cmp_gt_f32_e32 vcc, s55, v130
	v_mul_f32_e32 v131, 0x4b800000, v130
	s_lshl_b64 s[44:45], s[44:45], 10
	v_cndmask_b32_e32 v130, v130, v131, vcc
	v_rsq_f32_e32 v130, v130
	s_nop 0
	v_mul_f32_e32 v131, 0x45800000, v130
	v_cndmask_b32_e32 v130, v130, v131, vcc
	v_pk_mul_f32 v[164:165], v[130:131], v[132:133] op_sel_hi:[0,1]
	v_pk_mul_f32 v[134:135], v[130:131], v[134:135] op_sel_hi:[0,1]
	v_pk_fma_f32 v[50:51], v[164:165], v[138:139], v[50:51]
	v_mov_b32_e32 v131, v1
	v_cvt_pk_fp8_f32 v131, v50, v51
	v_pk_fma_f32 v[52:53], v[134:135], v[136:137], v[52:53]
	v_cvt_pk_f16_f32 v50, v50, v51
	v_cvt_pk_f16_f32 v51, v52, v53
	v_cvt_pk_fp8_f32 v131, v52, v53 op_sel:[0,0,1]
	v_lshl_add_u64 v[132:133], v[114:115], 0, s[44:45]
	ds_write_b64 v141, v[50:51]
	s_and_b64 vcc, exec, s[10:11]
	v_mov_b64_e32 v[136:137], v[70:71]
	v_mov_b64_e32 v[134:135], v[72:73]
	v_mov_b32_e32 v50, v38
	v_mov_b32_e32 v51, v39
	v_mov_b32_e32 v52, v40
	v_mov_b32_e32 v53, v41
	global_store_dword v[132:133], v131, off
	s_cbranch_vccnz .LBB0_1633
	v_lshlrev_b32_e32 v50, 4, v56
	global_load_dwordx4 v[134:137], v50, s[42:43]
	global_load_dwordx4 v[164:167], v[64:65], off offset:1024
	s_nop 0
	global_load_dwordx4 v[50:53], v50, s[40:41]
	s_waitcnt vmcnt(2)
	v_pk_add_f32 v[134:135], v[134:135], 1.0 op_sel_hi:[1,0]
	v_pk_add_f32 v[138:139], v[136:137], 1.0 op_sel_hi:[1,0]
	s_waitcnt vmcnt(1)
	v_pk_mul_f32 v[136:137], v[164:165], v[134:135]
	v_pk_mul_f32 v[134:135], v[166:167], v[138:139]
	s_waitcnt vmcnt(0)
.LBB0_1633:
	v_mov_b32_e32 v131, v130
	v_pk_mul_f32 v[128:129], v[130:131], v[128:129]
	v_pk_mul_f32 v[126:127], v[130:131], v[126:127]
	v_pk_fma_f32 v[50:51], v[128:129], v[136:137], v[50:51]
	v_mov_b32_e32 v128, v1
	v_cvt_pk_fp8_f32 v128, v50, v51
	v_pk_fma_f32 v[52:53], v[126:127], v[134:135], v[52:53]
	v_cvt_pk_f16_f32 v50, v50, v51
	v_cvt_pk_f16_f32 v51, v52, v53
	v_cvt_pk_fp8_f32 v128, v52, v53 op_sel:[0,0,1]
	ds_write_b64 v142, v[50:51]
	s_and_b64 vcc, exec, s[10:11]
	v_mov_b64_e32 v[126:127], v[76:77]
	global_store_dword v[132:133], v128, off offset:256
	v_mov_b64_e32 v[128:129], v[74:75]
	v_mov_b32_e32 v50, v42
	v_mov_b32_e32 v51, v43
	v_mov_b32_e32 v52, v44
	v_mov_b32_e32 v53, v45
	s_cbranch_vccnz .LBB0_1635
	v_lshlrev_b32_e32 v50, 4, v58
	global_load_dwordx4 v[126:129], v50, s[42:43]
	global_load_dwordx4 v[134:137], v[64:65], off offset:2048
	s_nop 0
	global_load_dwordx4 v[50:53], v50, s[40:41]
	s_waitcnt vmcnt(2)
	v_pk_add_f32 v[126:127], v[126:127], 1.0 op_sel_hi:[1,0]
	v_pk_add_f32 v[138:139], v[128:129], 1.0 op_sel_hi:[1,0]
	s_waitcnt vmcnt(1)
	v_pk_mul_f32 v[128:129], v[134:135], v[126:127]
	v_pk_mul_f32 v[126:127], v[136:137], v[138:139]
	s_waitcnt vmcnt(0)
.LBB0_1635:
	v_pk_mul_f32 v[124:125], v[130:131], v[124:125]
	v_pk_mul_f32 v[122:123], v[130:131], v[122:123]
	v_pk_fma_f32 v[50:51], v[124:125], v[128:129], v[50:51]
	v_mov_b32_e32 v124, v1
	v_cvt_pk_fp8_f32 v124, v50, v51
	v_pk_fma_f32 v[52:53], v[122:123], v[126:127], v[52:53]
	v_cvt_pk_f16_f32 v50, v50, v51
	v_cvt_pk_f16_f32 v51, v52, v53
	v_cvt_pk_fp8_f32 v124, v52, v53 op_sel:[0,0,1]
	ds_write_b64 v143, v[50:51]
	s_and_b64 vcc, exec, s[10:11]
	v_mov_b64_e32 v[122:123], v[80:81]
	global_store_dword v[132:133], v124, off offset:512
	v_mov_b64_e32 v[124:125], v[78:79]
	v_mov_b32_e32 v50, v46
	v_mov_b32_e32 v51, v47
	v_mov_b32_e32 v52, v48
	v_mov_b32_e32 v53, v49
	s_cbranch_vccnz .LBB0_1637
	v_lshlrev_b32_e32 v50, 4, v60
	global_load_dwordx4 v[122:125], v50, s[42:43]
	global_load_dwordx4 v[126:129], v[64:65], off offset:3072
	s_nop 0
	global_load_dwordx4 v[50:53], v50, s[40:41]
	s_waitcnt vmcnt(2)
	v_pk_add_f32 v[122:123], v[122:123], 1.0 op_sel_hi:[1,0]
	v_pk_add_f32 v[134:135], v[124:125], 1.0 op_sel_hi:[1,0]
	s_waitcnt vmcnt(1)
	v_pk_mul_f32 v[124:125], v[126:127], v[122:123]
	v_pk_mul_f32 v[122:123], v[128:129], v[134:135]
	s_waitcnt vmcnt(0)
.LBB0_1637:
	v_pk_mul_f32 v[120:121], v[130:131], v[120:121]
	v_pk_mul_f32 v[118:119], v[130:131], v[118:119]
	v_pk_fma_f32 v[50:51], v[120:121], v[124:125], v[50:51]
	v_mov_b32_e32 v120, v1
	v_cvt_pk_fp8_f32 v120, v50, v51
	v_pk_fma_f32 v[52:53], v[118:119], v[122:123], v[52:53]
	v_cvt_pk_f16_f32 v50, v50, v51
	v_cvt_pk_f16_f32 v51, v52, v53
	v_cvt_pk_fp8_f32 v120, v52, v53 op_sel:[0,0,1]
	ds_write_b64 v144, v[50:51]
	global_store_dword v[132:133], v120, off offset:768
	s_add_i32 s40, s54, 1
	s_cmp_ge_i32 s40, s23
	s_cbranch_scc0 .LBB0_1656

.LBB0_1639:
	s_add_i32 s40, s52, s51
	s_waitcnt vmcnt(7)
	v_lshlrev_b32_e32 v132, 16, v98
	v_and_b32_e32 v133, 0xffff0000, v98
	s_waitcnt vmcnt(6)
	v_lshlrev_b32_e32 v128, 16, v100
	v_and_b32_e32 v129, 0xffff0000, v100
	s_add_i32 s44, s40, 2
	v_lshlrev_b32_e32 v134, 16, v99
	v_and_b32_e32 v135, 0xffff0000, v99
	v_pk_mul_f32 v[50:51], v[132:133], v[132:133]
	v_lshlrev_b32_e32 v126, 16, v101
	v_and_b32_e32 v127, 0xffff0000, v101
	v_pk_mul_f32 v[130:131], v[128:129], v[128:129]
	s_waitcnt vmcnt(5)
	v_lshlrev_b32_e32 v124, 16, v102
	v_and_b32_e32 v125, 0xffff0000, v102
	v_pk_mul_f32 v[52:53], v[134:135], v[134:135]
	v_pk_mul_f32 v[136:137], v[126:127], v[126:127]
	v_lshlrev_b32_e32 v122, 16, v103
	v_and_b32_e32 v123, 0xffff0000, v103
	v_pk_mul_f32 v[138:139], v[124:125], v[124:125]
	v_add_f32_e32 v130, v130, v131
	v_add_f32_e32 v50, v50, v51
	s_ashr_i32 s45, s44, 31
	v_pk_mul_f32 v[164:165], v[122:123], v[122:123]
	v_add_f32_e32 v130, v130, v136
	v_add_f32_e32 v50, v50, v52
	v_add_f32_e32 v51, v138, v139
	s_lshr_b32 s40, s45, 20
	s_waitcnt vmcnt(4)
	v_lshlrev_b32_e32 v120, 16, v104
	v_and_b32_e32 v121, 0xffff0000, v104
	v_add_f32_e32 v130, v137, v130
	v_add_f32_e32 v50, v53, v50
	v_add_f32_e32 v51, v51, v164
	s_add_i32 s40, s44, s40
	v_lshlrev_b32_e32 v118, 16, v105
	v_and_b32_e32 v119, 0xffff0000, v105
	v_pk_mul_f32 v[166:167], v[120:121], v[120:121]
	v_add_f32_e32 v50, v50, v130
	v_add_f32_e32 v51, v165, v51
	s_ashr_i32 s40, s40, 12
	v_pk_mul_f32 v[168:169], v[118:119], v[118:119]
	v_add_f32_e32 v50, v50, v51
	v_add_f32_e32 v51, v166, v167
	s_cmp_lt_i32 s44, 0x8000
	v_add_f32_e32 v51, v51, v168
	s_cselect_b32 s40, s40, 8
	v_add_f32_e32 v51, v169, v51
	s_ashr_i32 s41, s40, 31
	v_add_f32_e32 v50, v50, v51
	s_add_u32 s40, s49, s40
	s_addc_u32 s41, s48, s41
	v_add_f32_dpp v50, v50, v50 row_ror:1 row_mask:0xf bank_mask:0xf bound_ctrl:1
	s_mulk_i32 s41, 0x6000
	s_mul_hi_u32 s42, s40, 0x6000
	v_add_f32_dpp v50, v50, v50 row_ror:2 row_mask:0xf bank_mask:0xf bound_ctrl:1
	s_add_i32 s42, s42, s41
	s_mulk_i32 s40, 0x6000
	v_add_f32_dpp v50, v50, v50 row_ror:4 row_mask:0xf bank_mask:0xf bound_ctrl:1
	s_add_u32 s43, s30, s40
	s_addc_u32 s55, s31, s42
	v_add_f32_dpp v50, v50, v50 row_ror:8 row_mask:0xf bank_mask:0xf bound_ctrl:1
	v_mov_b32_e32 v51, v50
	s_nop 1
	v_permlane16_swap_b32_e32 v50, v51
	s_add_u32 s40, s43, 0x103000
	v_add_f32_e32 v130, v50, v51
	s_addc_u32 s41, s55, 0
	v_mov_b32_e32 v131, v130
	s_add_u32 s42, s43, 0x104000
	s_nop 0
	v_permlane32_swap_b32_e32 v130, v131
	s_addc_u32 s43, s55, 0
	s_and_b64 vcc, exec, s[10:11]
	v_mov_b64_e32 v[138:139], v[66:67]
	v_mov_b64_e32 v[136:137], v[68:69]
	v_mov_b32_e32 v50, v34
	v_mov_b32_e32 v51, v35
	v_mov_b32_e32 v52, v36
	v_mov_b32_e32 v53, v37
	s_cbranch_vccnz .LBB0_1641
	v_lshlrev_b32_e32 v50, 4, v54
	global_load_dwordx4 v[136:139], v50, s[42:43]
	global_load_dwordx4 v[164:167], v[64:65], off
	s_nop 0
	global_load_dwordx4 v[50:53], v50, s[40:41]
	s_waitcnt vmcnt(2)
	v_pk_add_f32 v[136:137], v[136:137], 1.0 op_sel_hi:[1,0]
	v_pk_add_f32 v[168:169], v[138:139], 1.0 op_sel_hi:[1,0]
	s_waitcnt vmcnt(1)
	v_pk_mul_f32 v[138:139], v[164:165], v[136:137]
	v_pk_mul_f32 v[136:137], v[166:167], v[168:169]
	s_waitcnt vmcnt(0)
.LBB0_1641:
	v_add_f32_e32 v130, v130, v131
	v_fmamk_f32 v130, v130, 0x3a800000, v237
	s_mov_b32 s55, 0x800000
	v_cmp_gt_f32_e32 vcc, s55, v130
	v_mul_f32_e32 v131, 0x4b800000, v130
	s_lshl_b64 s[44:45], s[44:45], 10
	v_cndmask_b32_e32 v130, v130, v131, vcc
	v_rsq_f32_e32 v130, v130
	s_nop 0
	v_mul_f32_e32 v131, 0x45800000, v130
	v_cndmask_b32_e32 v130, v130, v131, vcc
	v_pk_mul_f32 v[164:165], v[130:131], v[132:133] op_sel_hi:[0,1]
	v_pk_mul_f32 v[134:135], v[130:131], v[134:135] op_sel_hi:[0,1]
	v_pk_fma_f32 v[50:51], v[164:165], v[138:139], v[50:51]
	v_mov_b32_e32 v131, v1
	v_cvt_pk_fp8_f32 v131, v50, v51
	v_pk_fma_f32 v[52:53], v[134:135], v[136:137], v[52:53]
	v_cvt_pk_f16_f32 v50, v50, v51
	v_cvt_pk_f16_f32 v51, v52, v53
	v_cvt_pk_fp8_f32 v131, v52, v53 op_sel:[0,0,1]
	v_lshl_add_u64 v[132:133], v[114:115], 0, s[44:45]
	ds_write_b64 v149, v[50:51]
	s_and_b64 vcc, exec, s[10:11]
	v_mov_b64_e32 v[136:137], v[70:71]
	v_mov_b64_e32 v[134:135], v[72:73]
	v_mov_b32_e32 v50, v38
	v_mov_b32_e32 v51, v39
	v_mov_b32_e32 v52, v40
	v_mov_b32_e32 v53, v41
	global_store_dword v[132:133], v131, off
	s_cbranch_vccnz .LBB0_1643
	v_lshlrev_b32_e32 v50, 4, v56
	global_load_dwordx4 v[134:137], v50, s[42:43]
	global_load_dwordx4 v[164:167], v[64:65], off offset:1024
	s_nop 0
	global_load_dwordx4 v[50:53], v50, s[40:41]
	s_waitcnt vmcnt(2)
	v_pk_add_f32 v[134:135], v[134:135], 1.0 op_sel_hi:[1,0]
	v_pk_add_f32 v[138:139], v[136:137], 1.0 op_sel_hi:[1,0]
	s_waitcnt vmcnt(1)
	v_pk_mul_f32 v[136:137], v[164:165], v[134:135]
	v_pk_mul_f32 v[134:135], v[166:167], v[138:139]
	s_waitcnt vmcnt(0)
.LBB0_1643:
	v_mov_b32_e32 v131, v130
	v_pk_mul_f32 v[128:129], v[130:131], v[128:129]
	v_pk_mul_f32 v[126:127], v[130:131], v[126:127]
	v_pk_fma_f32 v[50:51], v[128:129], v[136:137], v[50:51]
	v_mov_b32_e32 v128, v1
	v_cvt_pk_fp8_f32 v128, v50, v51
	v_pk_fma_f32 v[52:53], v[126:127], v[134:135], v[52:53]
	v_cvt_pk_f16_f32 v50, v50, v51
	v_cvt_pk_f16_f32 v51, v52, v53
	v_cvt_pk_fp8_f32 v128, v52, v53 op_sel:[0,0,1]
	ds_write_b64 v150, v[50:51]
	s_and_b64 vcc, exec, s[10:11]
	v_mov_b64_e32 v[126:127], v[76:77]
	global_store_dword v[132:133], v128, off offset:256
	v_mov_b64_e32 v[128:129], v[74:75]
	v_mov_b32_e32 v50, v42
	v_mov_b32_e32 v51, v43
	v_mov_b32_e32 v52, v44
	v_mov_b32_e32 v53, v45
	s_cbranch_vccnz .LBB0_1645
	v_lshlrev_b32_e32 v50, 4, v58
	global_load_dwordx4 v[126:129], v50, s[42:43]
	global_load_dwordx4 v[134:137], v[64:65], off offset:2048
	s_nop 0
	global_load_dwordx4 v[50:53], v50, s[40:41]
	s_waitcnt vmcnt(2)
	v_pk_add_f32 v[126:127], v[126:127], 1.0 op_sel_hi:[1,0]
	v_pk_add_f32 v[138:139], v[128:129], 1.0 op_sel_hi:[1,0]
	s_waitcnt vmcnt(1)
	v_pk_mul_f32 v[128:129], v[134:135], v[126:127]
	v_pk_mul_f32 v[126:127], v[136:137], v[138:139]
	s_waitcnt vmcnt(0)
.LBB0_1645:
	v_pk_mul_f32 v[124:125], v[130:131], v[124:125]
	v_pk_mul_f32 v[122:123], v[130:131], v[122:123]
	v_pk_fma_f32 v[50:51], v[124:125], v[128:129], v[50:51]
	v_mov_b32_e32 v124, v1
	v_cvt_pk_fp8_f32 v124, v50, v51
	v_pk_fma_f32 v[52:53], v[122:123], v[126:127], v[52:53]
	v_cvt_pk_f16_f32 v50, v50, v51
	v_cvt_pk_f16_f32 v51, v52, v53
	v_cvt_pk_fp8_f32 v124, v52, v53 op_sel:[0,0,1]
	ds_write_b64 v151, v[50:51]
	s_and_b64 vcc, exec, s[10:11]
	v_mov_b64_e32 v[122:123], v[80:81]
	global_store_dword v[132:133], v124, off offset:512
	v_mov_b64_e32 v[124:125], v[78:79]
	v_mov_b32_e32 v50, v46
	v_mov_b32_e32 v51, v47
	v_mov_b32_e32 v52, v48
	v_mov_b32_e32 v53, v49
	s_cbranch_vccnz .LBB0_1647
	v_lshlrev_b32_e32 v50, 4, v60
	global_load_dwordx4 v[122:125], v50, s[42:43]
	global_load_dwordx4 v[126:129], v[64:65], off offset:3072
	s_nop 0
	global_load_dwordx4 v[50:53], v50, s[40:41]
	s_waitcnt vmcnt(2)
	v_pk_add_f32 v[122:123], v[122:123], 1.0 op_sel_hi:[1,0]
	v_pk_add_f32 v[134:135], v[124:125], 1.0 op_sel_hi:[1,0]
	s_waitcnt vmcnt(1)
	v_pk_mul_f32 v[124:125], v[126:127], v[122:123]
	v_pk_mul_f32 v[122:123], v[128:129], v[134:135]
	s_waitcnt vmcnt(0)
.LBB0_1647:
	v_pk_mul_f32 v[120:121], v[130:131], v[120:121]
	v_pk_mul_f32 v[118:119], v[130:131], v[118:119]
	v_pk_fma_f32 v[50:51], v[120:121], v[124:125], v[50:51]
	v_mov_b32_e32 v120, v1
	v_cvt_pk_fp8_f32 v120, v50, v51
	v_pk_fma_f32 v[52:53], v[118:119], v[122:123], v[52:53]
	v_cvt_pk_f16_f32 v50, v50, v51
	v_cvt_pk_f16_f32 v51, v52, v53
	v_cvt_pk_fp8_f32 v120, v52, v53 op_sel:[0,0,1]
	ds_write_b64 v152, v[50:51]
	global_store_dword v[132:133], v120, off offset:768
	s_add_i32 s40, s54, 3
	s_cmp_ge_i32 s40, s23
	s_cbranch_scc0 .LBB0_1666

.LBB0_1656:
	s_add_i32 s40, s52, s51
	s_waitcnt vmcnt(11)
	v_lshlrev_b32_e32 v132, 16, v90
	v_and_b32_e32 v133, 0xffff0000, v90
	s_waitcnt vmcnt(10)
	v_lshlrev_b32_e32 v128, 16, v92
	v_and_b32_e32 v129, 0xffff0000, v92
	s_add_i32 s44, s40, 1
	v_lshlrev_b32_e32 v134, 16, v91
	v_and_b32_e32 v135, 0xffff0000, v91
	v_pk_mul_f32 v[50:51], v[132:133], v[132:133]
	v_lshlrev_b32_e32 v126, 16, v93
	v_and_b32_e32 v127, 0xffff0000, v93
	v_pk_mul_f32 v[130:131], v[128:129], v[128:129]
	s_waitcnt vmcnt(9)
	v_lshlrev_b32_e32 v124, 16, v94
	v_and_b32_e32 v125, 0xffff0000, v94
	v_pk_mul_f32 v[52:53], v[134:135], v[134:135]
	v_pk_mul_f32 v[136:137], v[126:127], v[126:127]
	v_lshlrev_b32_e32 v122, 16, v95
	v_and_b32_e32 v123, 0xffff0000, v95
	v_pk_mul_f32 v[138:139], v[124:125], v[124:125]
	v_add_f32_e32 v130, v130, v131
	v_add_f32_e32 v50, v50, v51
	s_ashr_i32 s45, s44, 31
	v_pk_mul_f32 v[164:165], v[122:123], v[122:123]
	v_add_f32_e32 v130, v130, v136
	v_add_f32_e32 v50, v50, v52
	v_add_f32_e32 v51, v138, v139
	s_lshr_b32 s40, s45, 20
	s_waitcnt vmcnt(8)
	v_lshlrev_b32_e32 v120, 16, v96
	v_and_b32_e32 v121, 0xffff0000, v96
	v_add_f32_e32 v130, v137, v130
	v_add_f32_e32 v50, v53, v50
	v_add_f32_e32 v51, v51, v164
	s_add_i32 s40, s44, s40
	v_lshlrev_b32_e32 v118, 16, v97
	v_and_b32_e32 v119, 0xffff0000, v97
	v_pk_mul_f32 v[166:167], v[120:121], v[120:121]
	v_add_f32_e32 v50, v50, v130
	v_add_f32_e32 v51, v165, v51
	s_ashr_i32 s40, s40, 12
	v_pk_mul_f32 v[168:169], v[118:119], v[118:119]
	v_add_f32_e32 v50, v50, v51
	v_add_f32_e32 v51, v166, v167
	s_cmp_lt_i32 s44, 0x8000
	v_add_f32_e32 v51, v51, v168
	s_cselect_b32 s40, s40, 8
	v_add_f32_e32 v51, v169, v51
	s_ashr_i32 s41, s40, 31
	v_add_f32_e32 v50, v50, v51
	s_add_u32 s40, s49, s40
	s_addc_u32 s41, s48, s41
	v_add_f32_dpp v50, v50, v50 row_ror:1 row_mask:0xf bank_mask:0xf bound_ctrl:1
	s_mulk_i32 s41, 0x6000
	s_mul_hi_u32 s42, s40, 0x6000
	v_add_f32_dpp v50, v50, v50 row_ror:2 row_mask:0xf bank_mask:0xf bound_ctrl:1
	s_add_i32 s42, s42, s41
	s_mulk_i32 s40, 0x6000
	v_add_f32_dpp v50, v50, v50 row_ror:4 row_mask:0xf bank_mask:0xf bound_ctrl:1
	s_add_u32 s43, s30, s40
	s_addc_u32 s55, s31, s42
	v_add_f32_dpp v50, v50, v50 row_ror:8 row_mask:0xf bank_mask:0xf bound_ctrl:1
	v_mov_b32_e32 v51, v50
	s_nop 1
	v_permlane16_swap_b32_e32 v50, v51
	s_add_u32 s40, s43, 0x103000
	v_add_f32_e32 v130, v50, v51
	s_addc_u32 s41, s55, 0
	v_mov_b32_e32 v131, v130
	s_add_u32 s42, s43, 0x104000
	s_nop 0
	v_permlane32_swap_b32_e32 v130, v131
	s_addc_u32 s43, s55, 0
	s_and_b64 vcc, exec, s[10:11]
	v_mov_b64_e32 v[138:139], v[66:67]
	v_mov_b64_e32 v[136:137], v[68:69]
	v_mov_b32_e32 v50, v34
	v_mov_b32_e32 v51, v35
	v_mov_b32_e32 v52, v36
	v_mov_b32_e32 v53, v37
	s_cbranch_vccnz .LBB0_1658
	v_lshlrev_b32_e32 v50, 4, v54
	global_load_dwordx4 v[136:139], v50, s[42:43]
	global_load_dwordx4 v[164:167], v[64:65], off
	s_nop 0
	global_load_dwordx4 v[50:53], v50, s[40:41]
	s_waitcnt vmcnt(2)
	v_pk_add_f32 v[136:137], v[136:137], 1.0 op_sel_hi:[1,0]
	v_pk_add_f32 v[168:169], v[138:139], 1.0 op_sel_hi:[1,0]
	s_waitcnt vmcnt(1)
	v_pk_mul_f32 v[138:139], v[164:165], v[136:137]
	v_pk_mul_f32 v[136:137], v[166:167], v[168:169]
	s_waitcnt vmcnt(0)
.LBB0_1658:
	v_add_f32_e32 v130, v130, v131
	v_fmamk_f32 v130, v130, 0x3a800000, v237
	s_mov_b32 s55, 0x800000
	v_cmp_gt_f32_e32 vcc, s55, v130
	v_mul_f32_e32 v131, 0x4b800000, v130
	s_lshl_b64 s[44:45], s[44:45], 10
	v_cndmask_b32_e32 v130, v130, v131, vcc
	v_rsq_f32_e32 v130, v130
	s_nop 0
	v_mul_f32_e32 v131, 0x45800000, v130
	v_cndmask_b32_e32 v130, v130, v131, vcc
	v_pk_mul_f32 v[164:165], v[130:131], v[132:133] op_sel_hi:[0,1]
	v_pk_mul_f32 v[134:135], v[130:131], v[134:135] op_sel_hi:[0,1]
	v_pk_fma_f32 v[50:51], v[164:165], v[138:139], v[50:51]
	v_mov_b32_e32 v131, v1
	v_cvt_pk_fp8_f32 v131, v50, v51
	v_pk_fma_f32 v[52:53], v[134:135], v[136:137], v[52:53]
	v_cvt_pk_f16_f32 v50, v50, v51
	v_cvt_pk_f16_f32 v51, v52, v53
	v_cvt_pk_fp8_f32 v131, v52, v53 op_sel:[0,0,1]
	v_lshl_add_u64 v[132:133], v[114:115], 0, s[44:45]
	ds_write_b64 v145, v[50:51]
	s_and_b64 vcc, exec, s[10:11]
	v_mov_b64_e32 v[136:137], v[70:71]
	v_mov_b64_e32 v[134:135], v[72:73]
	v_mov_b32_e32 v50, v38
	v_mov_b32_e32 v51, v39
	v_mov_b32_e32 v52, v40
	v_mov_b32_e32 v53, v41
	global_store_dword v[132:133], v131, off
	s_cbranch_vccnz .LBB0_1660
	v_lshlrev_b32_e32 v50, 4, v56
	global_load_dwordx4 v[134:137], v50, s[42:43]
	global_load_dwordx4 v[164:167], v[64:65], off offset:1024
	s_nop 0
	global_load_dwordx4 v[50:53], v50, s[40:41]
	s_waitcnt vmcnt(2)
	v_pk_add_f32 v[134:135], v[134:135], 1.0 op_sel_hi:[1,0]
	v_pk_add_f32 v[138:139], v[136:137], 1.0 op_sel_hi:[1,0]
	s_waitcnt vmcnt(1)
	v_pk_mul_f32 v[136:137], v[164:165], v[134:135]
	v_pk_mul_f32 v[134:135], v[166:167], v[138:139]
	s_waitcnt vmcnt(0)
.LBB0_1660:
	v_mov_b32_e32 v131, v130
	v_pk_mul_f32 v[128:129], v[130:131], v[128:129]
	v_pk_mul_f32 v[126:127], v[130:131], v[126:127]
	v_pk_fma_f32 v[50:51], v[128:129], v[136:137], v[50:51]
	v_mov_b32_e32 v128, v1
	v_cvt_pk_fp8_f32 v128, v50, v51
	v_pk_fma_f32 v[52:53], v[126:127], v[134:135], v[52:53]
	v_cvt_pk_f16_f32 v50, v50, v51
	v_cvt_pk_f16_f32 v51, v52, v53
	v_cvt_pk_fp8_f32 v128, v52, v53 op_sel:[0,0,1]
	ds_write_b64 v146, v[50:51]
	s_and_b64 vcc, exec, s[10:11]
	v_mov_b64_e32 v[126:127], v[76:77]
	global_store_dword v[132:133], v128, off offset:256
	v_mov_b64_e32 v[128:129], v[74:75]
	v_mov_b32_e32 v50, v42
	v_mov_b32_e32 v51, v43
	v_mov_b32_e32 v52, v44
	v_mov_b32_e32 v53, v45
	s_cbranch_vccnz .LBB0_1662
	v_lshlrev_b32_e32 v50, 4, v58
	global_load_dwordx4 v[126:129], v50, s[42:43]
	global_load_dwordx4 v[134:137], v[64:65], off offset:2048
	s_nop 0
	global_load_dwordx4 v[50:53], v50, s[40:41]
	s_waitcnt vmcnt(2)
	v_pk_add_f32 v[126:127], v[126:127], 1.0 op_sel_hi:[1,0]
	v_pk_add_f32 v[138:139], v[128:129], 1.0 op_sel_hi:[1,0]
	s_waitcnt vmcnt(1)
	v_pk_mul_f32 v[128:129], v[134:135], v[126:127]
	v_pk_mul_f32 v[126:127], v[136:137], v[138:139]
	s_waitcnt vmcnt(0)
.LBB0_1662:
	v_pk_mul_f32 v[124:125], v[130:131], v[124:125]
	v_pk_mul_f32 v[122:123], v[130:131], v[122:123]
	v_pk_fma_f32 v[50:51], v[124:125], v[128:129], v[50:51]
	v_mov_b32_e32 v124, v1
	v_cvt_pk_fp8_f32 v124, v50, v51
	v_pk_fma_f32 v[52:53], v[122:123], v[126:127], v[52:53]
	v_cvt_pk_f16_f32 v50, v50, v51
	v_cvt_pk_f16_f32 v51, v52, v53
	v_cvt_pk_fp8_f32 v124, v52, v53 op_sel:[0,0,1]
	ds_write_b64 v147, v[50:51]
	s_and_b64 vcc, exec, s[10:11]
	v_mov_b64_e32 v[122:123], v[80:81]
	global_store_dword v[132:133], v124, off offset:512
	v_mov_b64_e32 v[124:125], v[78:79]
	v_mov_b32_e32 v50, v46
	v_mov_b32_e32 v51, v47
	v_mov_b32_e32 v52, v48
	v_mov_b32_e32 v53, v49
	s_cbranch_vccnz .LBB0_1664
	v_lshlrev_b32_e32 v50, 4, v60
	global_load_dwordx4 v[122:125], v50, s[42:43]
	global_load_dwordx4 v[126:129], v[64:65], off offset:3072
	s_nop 0
	global_load_dwordx4 v[50:53], v50, s[40:41]
	s_waitcnt vmcnt(2)
	v_pk_add_f32 v[122:123], v[122:123], 1.0 op_sel_hi:[1,0]
	v_pk_add_f32 v[134:135], v[124:125], 1.0 op_sel_hi:[1,0]
	s_waitcnt vmcnt(1)
	v_pk_mul_f32 v[124:125], v[126:127], v[122:123]
	v_pk_mul_f32 v[122:123], v[128:129], v[134:135]
	s_waitcnt vmcnt(0)
.LBB0_1664:
	v_pk_mul_f32 v[120:121], v[130:131], v[120:121]
	v_pk_mul_f32 v[118:119], v[130:131], v[118:119]
	v_pk_fma_f32 v[50:51], v[120:121], v[124:125], v[50:51]
	v_mov_b32_e32 v120, v1
	v_cvt_pk_fp8_f32 v120, v50, v51
	v_pk_fma_f32 v[52:53], v[118:119], v[122:123], v[52:53]
	v_cvt_pk_f16_f32 v50, v50, v51
	v_cvt_pk_f16_f32 v51, v52, v53
	v_cvt_pk_fp8_f32 v120, v52, v53 op_sel:[0,0,1]
	ds_write_b64 v148, v[50:51]
	global_store_dword v[132:133], v120, off offset:768
	s_add_i32 s40, s54, 2
	s_cmp_ge_i32 s40, s23
	s_cbranch_scc0 .LBB0_1639

.LBB0_1666:
	s_add_i32 s40, s52, s51
	s_waitcnt vmcnt(3)
	v_lshlrev_b32_e32 v132, 16, v106
	v_and_b32_e32 v133, 0xffff0000, v106
	s_waitcnt vmcnt(2)
	v_lshlrev_b32_e32 v128, 16, v108
	v_and_b32_e32 v129, 0xffff0000, v108
	s_add_i32 s44, s40, 3
	v_lshlrev_b32_e32 v134, 16, v107
	v_and_b32_e32 v135, 0xffff0000, v107
	v_pk_mul_f32 v[50:51], v[132:133], v[132:133]
	v_lshlrev_b32_e32 v126, 16, v109
	v_and_b32_e32 v127, 0xffff0000, v109
	v_pk_mul_f32 v[130:131], v[128:129], v[128:129]
	s_waitcnt vmcnt(1)
	v_lshlrev_b32_e32 v124, 16, v110
	v_and_b32_e32 v125, 0xffff0000, v110
	v_pk_mul_f32 v[52:53], v[134:135], v[134:135]
	v_pk_mul_f32 v[136:137], v[126:127], v[126:127]
	v_lshlrev_b32_e32 v122, 16, v111
	v_and_b32_e32 v123, 0xffff0000, v111
	v_pk_mul_f32 v[138:139], v[124:125], v[124:125]
	v_add_f32_e32 v130, v130, v131
	v_add_f32_e32 v50, v50, v51
	s_ashr_i32 s45, s44, 31
	v_pk_mul_f32 v[164:165], v[122:123], v[122:123]
	v_add_f32_e32 v130, v130, v136
	v_add_f32_e32 v50, v50, v52
	v_add_f32_e32 v51, v138, v139
	s_lshr_b32 s40, s45, 20
	s_waitcnt vmcnt(0)
	v_lshlrev_b32_e32 v120, 16, v112
	v_and_b32_e32 v121, 0xffff0000, v112
	v_add_f32_e32 v130, v137, v130
	v_add_f32_e32 v50, v53, v50
	v_add_f32_e32 v51, v51, v164
	s_add_i32 s40, s44, s40
	v_lshlrev_b32_e32 v118, 16, v113
	v_and_b32_e32 v119, 0xffff0000, v113
	v_pk_mul_f32 v[166:167], v[120:121], v[120:121]
	v_add_f32_e32 v50, v50, v130
	v_add_f32_e32 v51, v165, v51
	s_ashr_i32 s40, s40, 12
	v_pk_mul_f32 v[168:169], v[118:119], v[118:119]
	v_add_f32_e32 v50, v50, v51
	v_add_f32_e32 v51, v166, v167
	s_cmp_lt_i32 s44, 0x8000
	v_add_f32_e32 v51, v51, v168
	s_cselect_b32 s40, s40, 8
	v_add_f32_e32 v51, v169, v51
	s_ashr_i32 s41, s40, 31
	v_add_f32_e32 v50, v50, v51
	s_add_u32 s40, s49, s40
	s_addc_u32 s41, s48, s41
	v_add_f32_dpp v50, v50, v50 row_ror:1 row_mask:0xf bank_mask:0xf bound_ctrl:1
	s_mulk_i32 s41, 0x6000
	s_mul_hi_u32 s42, s40, 0x6000
	v_add_f32_dpp v50, v50, v50 row_ror:2 row_mask:0xf bank_mask:0xf bound_ctrl:1
	s_add_i32 s42, s42, s41
	s_mulk_i32 s40, 0x6000
	v_add_f32_dpp v50, v50, v50 row_ror:4 row_mask:0xf bank_mask:0xf bound_ctrl:1
	s_add_u32 s43, s30, s40
	s_addc_u32 s55, s31, s42
	v_add_f32_dpp v50, v50, v50 row_ror:8 row_mask:0xf bank_mask:0xf bound_ctrl:1
	v_mov_b32_e32 v51, v50
	s_nop 1
	v_permlane16_swap_b32_e32 v50, v51
	s_add_u32 s40, s43, 0x103000
	v_add_f32_e32 v130, v50, v51
	s_addc_u32 s41, s55, 0
	v_mov_b32_e32 v131, v130
	s_add_u32 s42, s43, 0x104000
	s_nop 0
	v_permlane32_swap_b32_e32 v130, v131
	s_addc_u32 s43, s55, 0
	s_and_b64 vcc, exec, s[10:11]
	v_mov_b64_e32 v[138:139], v[66:67]
	v_mov_b64_e32 v[136:137], v[68:69]
	v_mov_b32_e32 v50, v34
	v_mov_b32_e32 v51, v35
	v_mov_b32_e32 v52, v36
	v_mov_b32_e32 v53, v37
	s_cbranch_vccnz .LBB0_1668
	v_lshlrev_b32_e32 v50, 4, v54
	global_load_dwordx4 v[136:139], v50, s[42:43]
	global_load_dwordx4 v[164:167], v[64:65], off
	s_nop 0
	global_load_dwordx4 v[50:53], v50, s[40:41]
	s_waitcnt vmcnt(2)
	v_pk_add_f32 v[136:137], v[136:137], 1.0 op_sel_hi:[1,0]
	v_pk_add_f32 v[168:169], v[138:139], 1.0 op_sel_hi:[1,0]
	s_waitcnt vmcnt(1)
	v_pk_mul_f32 v[138:139], v[164:165], v[136:137]
	v_pk_mul_f32 v[136:137], v[166:167], v[168:169]
	s_waitcnt vmcnt(0)
.LBB0_1668:
	v_add_f32_e32 v130, v130, v131
	v_fmamk_f32 v130, v130, 0x3a800000, v237
	s_mov_b32 s55, 0x800000
	v_cmp_gt_f32_e32 vcc, s55, v130
	v_mul_f32_e32 v131, 0x4b800000, v130
	s_lshl_b64 s[44:45], s[44:45], 10
	v_cndmask_b32_e32 v130, v130, v131, vcc
	v_rsq_f32_e32 v130, v130
	s_nop 0
	v_mul_f32_e32 v131, 0x45800000, v130
	v_cndmask_b32_e32 v130, v130, v131, vcc
	v_pk_mul_f32 v[164:165], v[130:131], v[132:133] op_sel_hi:[0,1]
	v_pk_mul_f32 v[134:135], v[130:131], v[134:135] op_sel_hi:[0,1]
	v_pk_fma_f32 v[50:51], v[164:165], v[138:139], v[50:51]
	v_mov_b32_e32 v131, v1
	v_cvt_pk_fp8_f32 v131, v50, v51
	v_pk_fma_f32 v[52:53], v[134:135], v[136:137], v[52:53]
	v_cvt_pk_f16_f32 v50, v50, v51
	v_cvt_pk_f16_f32 v51, v52, v53
	v_cvt_pk_fp8_f32 v131, v52, v53 op_sel:[0,0,1]
	v_lshl_add_u64 v[132:133], v[114:115], 0, s[44:45]
	ds_write_b64 v153, v[50:51]
	s_and_b64 vcc, exec, s[10:11]
	v_mov_b64_e32 v[136:137], v[70:71]
	v_mov_b64_e32 v[134:135], v[72:73]
	v_mov_b32_e32 v50, v38
	v_mov_b32_e32 v51, v39
	v_mov_b32_e32 v52, v40
	v_mov_b32_e32 v53, v41
	global_store_dword v[132:133], v131, off
	s_cbranch_vccnz .LBB0_1670
	v_lshlrev_b32_e32 v50, 4, v56
	global_load_dwordx4 v[134:137], v50, s[42:43]
	global_load_dwordx4 v[164:167], v[64:65], off offset:1024
	s_nop 0
	global_load_dwordx4 v[50:53], v50, s[40:41]
	s_waitcnt vmcnt(2)
	v_pk_add_f32 v[134:135], v[134:135], 1.0 op_sel_hi:[1,0]
	v_pk_add_f32 v[138:139], v[136:137], 1.0 op_sel_hi:[1,0]
	s_waitcnt vmcnt(1)
	v_pk_mul_f32 v[136:137], v[164:165], v[134:135]
	v_pk_mul_f32 v[134:135], v[166:167], v[138:139]
	s_waitcnt vmcnt(0)
.LBB0_1670:
	v_mov_b32_e32 v131, v130
	v_pk_mul_f32 v[128:129], v[130:131], v[128:129]
	v_pk_mul_f32 v[126:127], v[130:131], v[126:127]
	v_pk_fma_f32 v[50:51], v[128:129], v[136:137], v[50:51]
	v_mov_b32_e32 v128, v1
	v_cvt_pk_fp8_f32 v128, v50, v51
	v_pk_fma_f32 v[52:53], v[126:127], v[134:135], v[52:53]
	v_cvt_pk_f16_f32 v50, v50, v51
	v_cvt_pk_f16_f32 v51, v52, v53
	v_cvt_pk_fp8_f32 v128, v52, v53 op_sel:[0,0,1]
	ds_write_b64 v154, v[50:51]
	s_and_b64 vcc, exec, s[10:11]
	v_mov_b64_e32 v[126:127], v[76:77]
	global_store_dword v[132:133], v128, off offset:256
	v_mov_b64_e32 v[128:129], v[74:75]
	v_mov_b32_e32 v50, v42
	v_mov_b32_e32 v51, v43
	v_mov_b32_e32 v52, v44
	v_mov_b32_e32 v53, v45
	s_cbranch_vccnz .LBB0_1672
	v_lshlrev_b32_e32 v50, 4, v58
	global_load_dwordx4 v[126:129], v50, s[42:43]
	global_load_dwordx4 v[134:137], v[64:65], off offset:2048
	s_nop 0
	global_load_dwordx4 v[50:53], v50, s[40:41]
	s_waitcnt vmcnt(2)
	v_pk_add_f32 v[126:127], v[126:127], 1.0 op_sel_hi:[1,0]
	v_pk_add_f32 v[138:139], v[128:129], 1.0 op_sel_hi:[1,0]
	s_waitcnt vmcnt(1)
	v_pk_mul_f32 v[128:129], v[134:135], v[126:127]
	v_pk_mul_f32 v[126:127], v[136:137], v[138:139]
	s_waitcnt vmcnt(0)
.LBB0_1672:
	v_pk_mul_f32 v[124:125], v[130:131], v[124:125]
	v_pk_mul_f32 v[122:123], v[130:131], v[122:123]
	v_pk_fma_f32 v[50:51], v[124:125], v[128:129], v[50:51]
	v_mov_b32_e32 v124, v1
	v_cvt_pk_fp8_f32 v124, v50, v51
	v_pk_fma_f32 v[52:53], v[122:123], v[126:127], v[52:53]
	v_cvt_pk_f16_f32 v50, v50, v51
	v_cvt_pk_f16_f32 v51, v52, v53
	v_cvt_pk_fp8_f32 v124, v52, v53 op_sel:[0,0,1]
	ds_write_b64 v155, v[50:51]
	s_and_b64 vcc, exec, s[10:11]
	v_mov_b64_e32 v[122:123], v[80:81]
	global_store_dword v[132:133], v124, off offset:512
	v_mov_b64_e32 v[124:125], v[78:79]
	v_mov_b32_e32 v50, v46
	v_mov_b32_e32 v51, v47
	v_mov_b32_e32 v52, v48
	v_mov_b32_e32 v53, v49
	s_cbranch_vccnz .LBB0_1674
	v_lshlrev_b32_e32 v50, 4, v60
	global_load_dwordx4 v[122:125], v50, s[42:43]
	global_load_dwordx4 v[126:129], v[64:65], off offset:3072
	s_nop 0
	global_load_dwordx4 v[50:53], v50, s[40:41]
	s_waitcnt vmcnt(2)
	v_pk_add_f32 v[122:123], v[122:123], 1.0 op_sel_hi:[1,0]
	v_pk_add_f32 v[134:135], v[124:125], 1.0 op_sel_hi:[1,0]
	s_waitcnt vmcnt(1)
	v_pk_mul_f32 v[124:125], v[126:127], v[122:123]
	v_pk_mul_f32 v[122:123], v[128:129], v[134:135]
	s_waitcnt vmcnt(0)
.LBB0_1674:
	v_pk_mul_f32 v[120:121], v[130:131], v[120:121]
	v_pk_mul_f32 v[118:119], v[130:131], v[118:119]
	v_pk_fma_f32 v[50:51], v[120:121], v[124:125], v[50:51]
	v_mov_b32_e32 v120, v1
	v_cvt_pk_fp8_f32 v120, v50, v51
	v_pk_fma_f32 v[52:53], v[118:119], v[122:123], v[52:53]
	v_cvt_pk_f16_f32 v50, v50, v51
	v_cvt_pk_f16_f32 v51, v52, v53
	v_cvt_pk_fp8_f32 v120, v52, v53 op_sel:[0,0,1]
	ds_write_b64 v156, v[50:51]
	global_store_dword v[132:133], v120, off offset:768
	s_cmp_lt_u32 s50, s46
	s_cbranch_scc1 .LBB0_1649
	s_branch .LBB0_1650
